# P6/P7 K-loops: every LDS-DMA piece now in scalar-base form (SP2 weight pieces and the SP1(t) row pieces too), 8 more 64-bit VALU adds per iteration replaced by 4 SALU; M0 wait states checked by lint
# speedup vs baseline: 1.0037x; 1.0037x over previous
.Lp6_first:
	ds_read_b128 v[18:21], v208
	ds_read_b128 v[22:25], v209
	ds_read_b128 v[26:29], v208 offset:2048
	ds_read_b128 v[30:33], v209 offset:2048
	ds_read_b128 v[2:5], v208 offset:16384
	ds_read_b128 v[6:9], v209 offset:16384
	ds_read_b128 v[10:13], v208 offset:18432
	ds_read_b128 v[14:17], v209 offset:18432
	s_add_u32 s84, s18, s40
	s_addc_u32 s85, s19, s41
	s_add_i32 m0, s35, 0x8000
	ds_read_b128 v[218:221], v211
	ds_read_b128 v[226:229], v211 offset:2048
	ds_read_b128 v[222:225], v212
	ds_read_b128 v[230:233], v212 offset:2048
	ds_read_b128 v[234:237], v211 offset:4096
	ds_read_b128 v[242:245], v211 offset:6144
	ds_read_b128 v[238:241], v212 offset:4096
	ds_read_b128 v[246:249], v212 offset:6144
	global_load_lds_dwordx4 v176, s[84:85]
	s_add_i32 m0, s35, 0xa000
	s_nop 0
	global_load_lds_dwordx4 v178, s[84:85]
	s_add_i32 m0, s35, 0xc000
	s_nop 0
	global_load_lds_dwordx4 v180, s[84:85]
	s_add_i32 m0, s35, 0xe000
	s_nop 0
	global_load_lds_dwordx4 v182, s[84:85]
	s_waitcnt vmcnt(8)
	s_waitcnt lgkmcnt(0)
	s_barrier
	s_setprio 1
	s_waitcnt lgkmcnt(0)
	v_mfma_f32_16x16x128_f8f6f4 v[158:161], v[18:25], v[218:225], 0
	s_add_u32 s44, s2, s40
	s_addc_u32 s45, s3, s41
	s_add_u32 s84, s44, 0x56800100
	s_addc_u32 s85, s45, 0
	v_mfma_f32_16x16x128_f8f6f4 v[154:157], v[26:33], v[218:225], 0
	s_and_b64 s[44:45], s[42:43], exec
	s_cselect_b32 s45, s9, s85
	s_cselect_b32 s44, s8, s84
	s_add_u32 s84, s29, s40
	v_mfma_f32_16x16x128_f8f6f4 v[150:153], v[18:25], v[226:233], 0
	s_addc_u32 s85, s37, s41
	s_and_b64 s[42:43], s[42:43], exec
	s_cselect_b32 s43, s31, s85
	s_cselect_b32 s42, s30, s84
	v_mfma_f32_16x16x128_f8f6f4 v[146:149], v[26:33], v[226:233], 0
	v_mfma_f32_16x16x128_f8f6f4 v[126:129], v[18:25], v[234:241], 0
	v_mfma_f32_16x16x128_f8f6f4 v[122:125], v[26:33], v[234:241], 0
	v_mfma_f32_16x16x128_f8f6f4 v[110:113], v[18:25], v[242:249], 0
	v_mfma_f32_16x16x128_f8f6f4 v[106:109], v[26:33], v[242:249], 0
	s_setprio 0
	s_setprio 1
	v_mfma_f32_16x16x128_f8f6f4 v[142:145], v[2:9], v[218:225], 0
	v_mfma_f32_16x16x128_f8f6f4 v[138:141], v[10:17], v[218:225], 0
	v_mfma_f32_16x16x128_f8f6f4 v[134:137], v[2:9], v[226:233], 0
	v_mfma_f32_16x16x128_f8f6f4 v[130:133], v[10:17], v[226:233], 0
	v_mfma_f32_16x16x128_f8f6f4 v[118:121], v[2:9], v[234:241], 0
	v_mfma_f32_16x16x128_f8f6f4 v[114:117], v[10:17], v[234:241], 0
	v_mfma_f32_16x16x128_f8f6f4 v[102:105], v[2:9], v[242:249], 0
	v_mfma_f32_16x16x128_f8f6f4 v[98:101], v[10:17], v[242:249], 0
	s_setprio 0
	s_barrier
	s_add_i32 s84, s68, s33
	s_mov_b32 m0, s84
	ds_read_b128 v[218:221], v211 offset:16384
	ds_read_b128 v[226:229], v211 offset:18432
	ds_read_b128 v[222:225], v212 offset:16384
	ds_read_b128 v[230:233], v212 offset:18432
	ds_read_b128 v[234:237], v211 offset:20480
	ds_read_b128 v[242:245], v211 offset:22528
	ds_read_b128 v[238:241], v212 offset:20480
	ds_read_b128 v[246:249], v212 offset:22528
	global_load_lds_dwordx4 v164, s[42:43]
	s_add_i32 m0, s84, 0x2000
	s_add_u32 s84, s42, 0x40000
	s_addc_u32 s85, s43, 0
	s_add_i32 s86, s70, s33
	global_load_lds_dwordx4 v166, s[42:43]
	s_mov_b32 m0, s86
	s_nop 0
	global_load_lds_dwordx4 v164, s[84:85]
	s_add_i32 m0, s86, 0x2000
	s_nop 0
	global_load_lds_dwordx4 v166, s[84:85]
	s_waitcnt vmcnt(6)
	s_waitcnt lgkmcnt(0)
	s_barrier
	s_setprio 1
	s_waitcnt lgkmcnt(0)
	v_mfma_f32_16x16x128_f8f6f4 v[94:97], v[18:25], v[218:225], 0
	v_mfma_f32_16x16x128_f8f6f4 v[90:93], v[26:33], v[218:225], 0
	v_mfma_f32_16x16x128_f8f6f4 v[78:81], v[18:25], v[226:233], 0
	v_mfma_f32_16x16x128_f8f6f4 v[74:77], v[26:33], v[226:233], 0
	v_mfma_f32_16x16x128_f8f6f4 v[62:65], v[18:25], v[234:241], 0
	v_mfma_f32_16x16x128_f8f6f4 v[58:61], v[26:33], v[234:241], 0
	v_mfma_f32_16x16x128_f8f6f4 v[46:49], v[18:25], v[242:249], 0
	v_mfma_f32_16x16x128_f8f6f4 v[42:45], v[26:33], v[242:249], 0
	s_setprio 0
	s_setprio 1
	v_mfma_f32_16x16x128_f8f6f4 v[86:89], v[2:9], v[218:225], 0
	v_mfma_f32_16x16x128_f8f6f4 v[82:85], v[10:17], v[218:225], 0
	v_mfma_f32_16x16x128_f8f6f4 v[70:73], v[2:9], v[226:233], 0
	v_mfma_f32_16x16x128_f8f6f4 v[66:69], v[10:17], v[226:233], 0
	v_mfma_f32_16x16x128_f8f6f4 v[54:57], v[2:9], v[234:241], 0
	v_mfma_f32_16x16x128_f8f6f4 v[50:53], v[10:17], v[234:241], 0
	v_mfma_f32_16x16x128_f8f6f4 v[38:41], v[2:9], v[242:249], 0
	v_mfma_f32_16x16x128_f8f6f4 v[34:37], v[10:17], v[242:249], 0
	s_setprio 0
	s_barrier
	s_branch .Lp6_blk3

.LBB0_777:
	s_cmp_eq_u32 s40, 0
	s_cbranch_scc1 .Lp6_first
	ds_read_b128 v[18:21], v208
	ds_read_b128 v[22:25], v209
	ds_read_b128 v[26:29], v208 offset:2048
	ds_read_b128 v[30:33], v209 offset:2048
	ds_read_b128 v[2:5], v208 offset:16384
	ds_read_b128 v[6:9], v209 offset:16384
	ds_read_b128 v[10:13], v208 offset:18432
	ds_read_b128 v[14:17], v209 offset:18432
	s_add_u32 s84, s18, s40
	s_addc_u32 s85, s19, s41
	s_add_i32 m0, s35, 0x8000
	ds_read_b128 v[218:221], v211
	ds_read_b128 v[226:229], v211 offset:2048
	ds_read_b128 v[222:225], v212
	ds_read_b128 v[230:233], v212 offset:2048
	ds_read_b128 v[234:237], v211 offset:4096
	ds_read_b128 v[242:245], v211 offset:6144
	ds_read_b128 v[238:241], v212 offset:4096
	ds_read_b128 v[246:249], v212 offset:6144
	global_load_lds_dwordx4 v176, s[84:85]
	s_add_i32 m0, s35, 0xa000
	s_nop 0
	global_load_lds_dwordx4 v178, s[84:85]
	s_add_i32 m0, s35, 0xc000
	s_nop 0
	global_load_lds_dwordx4 v180, s[84:85]
	s_add_i32 m0, s35, 0xe000
	s_nop 0
	global_load_lds_dwordx4 v182, s[84:85]
	s_waitcnt vmcnt(8)
	s_waitcnt lgkmcnt(0)
	s_barrier
	s_setprio 1
	s_waitcnt lgkmcnt(0)
	v_mfma_f32_16x16x128_f8f6f4 v[158:161], v[18:25], v[218:225], v[158:161]
	s_add_u32 s44, s2, s40
	s_addc_u32 s45, s3, s41
	s_add_u32 s84, s44, 0x56800100
	s_addc_u32 s85, s45, 0
	v_mfma_f32_16x16x128_f8f6f4 v[154:157], v[26:33], v[218:225], v[154:157]
	s_and_b64 s[44:45], s[42:43], exec
	s_cselect_b32 s45, s9, s85
	s_cselect_b32 s44, s8, s84
	s_add_u32 s84, s29, s40
	v_mfma_f32_16x16x128_f8f6f4 v[150:153], v[18:25], v[226:233], v[150:153]
	s_addc_u32 s85, s37, s41
	s_and_b64 s[42:43], s[42:43], exec
	s_cselect_b32 s43, s31, s85
	s_cselect_b32 s42, s30, s84
	v_mfma_f32_16x16x128_f8f6f4 v[146:149], v[26:33], v[226:233], v[146:149]
	v_mfma_f32_16x16x128_f8f6f4 v[126:129], v[18:25], v[234:241], v[126:129]
	v_mfma_f32_16x16x128_f8f6f4 v[122:125], v[26:33], v[234:241], v[122:125]
	v_mfma_f32_16x16x128_f8f6f4 v[110:113], v[18:25], v[242:249], v[110:113]
	v_mfma_f32_16x16x128_f8f6f4 v[106:109], v[26:33], v[242:249], v[106:109]
	s_setprio 0
	s_setprio 1
	v_mfma_f32_16x16x128_f8f6f4 v[142:145], v[2:9], v[218:225], v[142:145]
	v_mfma_f32_16x16x128_f8f6f4 v[138:141], v[10:17], v[218:225], v[138:141]
	v_mfma_f32_16x16x128_f8f6f4 v[134:137], v[2:9], v[226:233], v[134:137]
	v_mfma_f32_16x16x128_f8f6f4 v[130:133], v[10:17], v[226:233], v[130:133]
	v_mfma_f32_16x16x128_f8f6f4 v[118:121], v[2:9], v[234:241], v[118:121]
	v_mfma_f32_16x16x128_f8f6f4 v[114:117], v[10:17], v[234:241], v[114:117]
	v_mfma_f32_16x16x128_f8f6f4 v[102:105], v[2:9], v[242:249], v[102:105]
	v_mfma_f32_16x16x128_f8f6f4 v[98:101], v[10:17], v[242:249], v[98:101]
	s_setprio 0
	s_barrier
	s_add_i32 s84, s68, s33
	s_mov_b32 m0, s84
	ds_read_b128 v[218:221], v211 offset:16384
	ds_read_b128 v[226:229], v211 offset:18432
	ds_read_b128 v[222:225], v212 offset:16384
	ds_read_b128 v[230:233], v212 offset:18432
	ds_read_b128 v[234:237], v211 offset:20480
	ds_read_b128 v[242:245], v211 offset:22528
	ds_read_b128 v[238:241], v212 offset:20480
	ds_read_b128 v[246:249], v212 offset:22528
	global_load_lds_dwordx4 v164, s[42:43]
	s_add_i32 m0, s84, 0x2000
	s_add_u32 s84, s42, 0x40000
	s_addc_u32 s85, s43, 0
	s_add_i32 s86, s70, s33
	global_load_lds_dwordx4 v166, s[42:43]
	s_mov_b32 m0, s86
	s_nop 0
	global_load_lds_dwordx4 v164, s[84:85]
	s_add_i32 m0, s86, 0x2000
	s_nop 0
	global_load_lds_dwordx4 v166, s[84:85]
	s_waitcnt vmcnt(6)
	s_waitcnt lgkmcnt(0)
	s_barrier
	s_setprio 1
	s_waitcnt lgkmcnt(0)
	v_mfma_f32_16x16x128_f8f6f4 v[94:97], v[18:25], v[218:225], v[94:97]
	v_mfma_f32_16x16x128_f8f6f4 v[90:93], v[26:33], v[218:225], v[90:93]
	v_mfma_f32_16x16x128_f8f6f4 v[78:81], v[18:25], v[226:233], v[78:81]
	v_mfma_f32_16x16x128_f8f6f4 v[74:77], v[26:33], v[226:233], v[74:77]
	v_mfma_f32_16x16x128_f8f6f4 v[62:65], v[18:25], v[234:241], v[62:65]
	v_mfma_f32_16x16x128_f8f6f4 v[58:61], v[26:33], v[234:241], v[58:61]
	v_mfma_f32_16x16x128_f8f6f4 v[46:49], v[18:25], v[242:249], v[46:49]
	v_mfma_f32_16x16x128_f8f6f4 v[42:45], v[26:33], v[242:249], v[42:45]
	s_setprio 0
	s_setprio 1
	v_mfma_f32_16x16x128_f8f6f4 v[86:89], v[2:9], v[218:225], v[86:89]
	v_mfma_f32_16x16x128_f8f6f4 v[82:85], v[10:17], v[218:225], v[82:85]
	v_mfma_f32_16x16x128_f8f6f4 v[70:73], v[2:9], v[226:233], v[70:73]
	v_mfma_f32_16x16x128_f8f6f4 v[66:69], v[10:17], v[226:233], v[66:69]
	v_mfma_f32_16x16x128_f8f6f4 v[54:57], v[2:9], v[234:241], v[54:57]
	v_mfma_f32_16x16x128_f8f6f4 v[50:53], v[10:17], v[234:241], v[50:53]
	v_mfma_f32_16x16x128_f8f6f4 v[38:41], v[2:9], v[242:249], v[38:41]
	v_mfma_f32_16x16x128_f8f6f4 v[34:37], v[10:17], v[242:249], v[34:37]
	s_setprio 0
	s_barrier
.Lp6_blk3:
	ds_read_b128 v[2:5], v208 offset:32768
	ds_read_b128 v[6:9], v209 offset:32768
	ds_read_b128 v[10:13], v208 offset:34816
	ds_read_b128 v[14:17], v209 offset:34816
	ds_read_b128 v[18:21], v208 offset:49152
	ds_read_b128 v[22:25], v209 offset:49152
	ds_read_b128 v[26:29], v208 offset:51200
	ds_read_b128 v[30:33], v209 offset:51200
	s_mov_b32 m0, s35
	ds_read_b128 v[218:221], v211 offset:32768
	ds_read_b128 v[226:229], v211 offset:34816
	ds_read_b128 v[222:225], v212 offset:32768
	ds_read_b128 v[230:233], v212 offset:34816
	ds_read_b128 v[234:237], v211 offset:36864
	ds_read_b128 v[242:245], v211 offset:38912
	ds_read_b128 v[238:241], v212 offset:36864
	ds_read_b128 v[246:249], v212 offset:38912
	global_load_lds_dwordx4 v198, s[44:45]
	s_mov_b32 m0, s55
	s_nop 0
	global_load_lds_dwordx4 v196, s[44:45]
	s_mov_b32 m0, s64
	s_nop 0
	global_load_lds_dwordx4 v194, s[44:45]
	s_mov_b32 m0, s65
	s_nop 0
	global_load_lds_dwordx4 v192, s[44:45]
	s_waitcnt vmcnt(8)
	s_waitcnt lgkmcnt(0)
	s_barrier
	s_setprio 1
	s_waitcnt lgkmcnt(0)
	v_mfma_f32_16x16x128_f8f6f4 v[158:161], v[2:9], v[218:225], v[158:161]
	v_mfma_f32_16x16x128_f8f6f4 v[154:157], v[10:17], v[218:225], v[154:157]
	v_mfma_f32_16x16x128_f8f6f4 v[150:153], v[2:9], v[226:233], v[150:153]
	v_mfma_f32_16x16x128_f8f6f4 v[146:149], v[10:17], v[226:233], v[146:149]
	v_mfma_f32_16x16x128_f8f6f4 v[126:129], v[2:9], v[234:241], v[126:129]
	v_mfma_f32_16x16x128_f8f6f4 v[122:125], v[10:17], v[234:241], v[122:125]
	v_mfma_f32_16x16x128_f8f6f4 v[110:113], v[2:9], v[242:249], v[110:113]
	v_mfma_f32_16x16x128_f8f6f4 v[106:109], v[10:17], v[242:249], v[106:109]
	s_setprio 0
	s_setprio 1
	v_mfma_f32_16x16x128_f8f6f4 v[142:145], v[18:25], v[218:225], v[142:145]
	v_mfma_f32_16x16x128_f8f6f4 v[138:141], v[26:33], v[218:225], v[138:141]
	v_mfma_f32_16x16x128_f8f6f4 v[134:137], v[18:25], v[226:233], v[134:137]
	v_mfma_f32_16x16x128_f8f6f4 v[130:133], v[26:33], v[226:233], v[130:133]
	v_mfma_f32_16x16x128_f8f6f4 v[118:121], v[18:25], v[234:241], v[118:121]
	v_mfma_f32_16x16x128_f8f6f4 v[114:117], v[26:33], v[234:241], v[114:117]
	v_mfma_f32_16x16x128_f8f6f4 v[102:105], v[18:25], v[242:249], v[102:105]
	v_mfma_f32_16x16x128_f8f6f4 v[98:101], v[26:33], v[242:249], v[98:101]
	s_setprio 0
	s_barrier
	s_add_i32 s44, s72, s33
	s_add_u32 s84, s42, s10
	s_addc_u32 s85, s43, s11
	s_mov_b32 m0, s44
	ds_read_b128 v[192:195], v211 offset:49152
	ds_read_b128 v[218:221], v211 offset:51200
	ds_read_b128 v[196:199], v212 offset:49152
	ds_read_b128 v[222:225], v212 offset:51200
	ds_read_b128 v[226:229], v211 offset:53248
	ds_read_b128 v[234:237], v211 offset:55296
	ds_read_b128 v[230:233], v212 offset:53248
	ds_read_b128 v[238:241], v212 offset:55296
	global_load_lds_dwordx4 v164, s[84:85]
	s_add_i32 m0, s44, 0x2000
	s_add_u32 s42, s42, 0x40080
	s_addc_u32 s43, s43, 0
	s_add_i32 s44, s74, s33
	global_load_lds_dwordx4 v166, s[84:85]
	s_mov_b32 m0, s44
	s_nop 0
	global_load_lds_dwordx4 v164, s[42:43]
	s_add_i32 m0, s44, 0x2000
	s_nop 0
	global_load_lds_dwordx4 v166, s[42:43]
	s_waitcnt vmcnt(6)
	s_waitcnt lgkmcnt(0)
	s_barrier
	s_setprio 1
	s_waitcnt lgkmcnt(0)
	v_mfma_f32_16x16x128_f8f6f4 v[94:97], v[2:9], v[192:199], v[94:97]
	v_mfma_f32_16x16x128_f8f6f4 v[90:93], v[10:17], v[192:199], v[90:93]
	v_mfma_f32_16x16x128_f8f6f4 v[78:81], v[2:9], v[218:225], v[78:81]
	v_mfma_f32_16x16x128_f8f6f4 v[74:77], v[10:17], v[218:225], v[74:77]
	v_mfma_f32_16x16x128_f8f6f4 v[62:65], v[2:9], v[226:233], v[62:65]
	v_mfma_f32_16x16x128_f8f6f4 v[58:61], v[10:17], v[226:233], v[58:61]
	v_mfma_f32_16x16x128_f8f6f4 v[46:49], v[2:9], v[234:241], v[46:49]
	v_mfma_f32_16x16x128_f8f6f4 v[42:45], v[10:17], v[234:241], v[42:45]
	s_setprio 0
	s_setprio 1
	v_mfma_f32_16x16x128_f8f6f4 v[86:89], v[18:25], v[192:199], v[86:89]
	v_mfma_f32_16x16x128_f8f6f4 v[82:85], v[26:33], v[192:199], v[82:85]
	v_mfma_f32_16x16x128_f8f6f4 v[70:73], v[18:25], v[218:225], v[70:73]
	v_mfma_f32_16x16x128_f8f6f4 v[66:69], v[26:33], v[218:225], v[66:69]
	v_mfma_f32_16x16x128_f8f6f4 v[54:57], v[18:25], v[226:233], v[54:57]
	v_mfma_f32_16x16x128_f8f6f4 v[50:53], v[26:33], v[226:233], v[50:53]
	v_mfma_f32_16x16x128_f8f6f4 v[38:41], v[18:25], v[234:241], v[38:41]
	v_mfma_f32_16x16x128_f8f6f4 v[34:37], v[26:33], v[234:241], v[34:37]
	s_setprio 0
	s_barrier
	s_add_i32 s83, s83, 2
	s_add_u32 s40, s40, 0x100
	s_addc_u32 s41, s41, 0
	s_cmp_gt_u32 s83, 13
	s_cbranch_scc1 .LBB0_781

.Lp7_first:
	ds_read_b128 v[18:21], v210
	ds_read_b128 v[22:25], v211
	ds_read_b128 v[26:29], v210 offset:2048
	ds_read_b128 v[30:33], v211 offset:2048
	ds_read_b128 v[2:5], v210 offset:16384
	ds_read_b128 v[6:9], v211 offset:16384
	ds_read_b128 v[10:13], v210 offset:18432
	ds_read_b128 v[14:17], v211 offset:18432
	s_add_u32 s82, s20, s44
	s_addc_u32 s83, s21, s45
	s_add_i32 m0, s41, 0x8000
	ds_read_b128 v[220:223], v213
	ds_read_b128 v[228:231], v213 offset:2048
	ds_read_b128 v[224:227], v214
	ds_read_b128 v[232:235], v214 offset:2048
	ds_read_b128 v[236:239], v213 offset:4096
	ds_read_b128 v[244:247], v213 offset:6144
	ds_read_b128 v[240:243], v214 offset:4096
	ds_read_b128 v[248:251], v214 offset:6144
	global_load_lds_dwordx4 v166, s[82:83]
	s_add_i32 m0, s41, 0xa000
	s_nop 0
	global_load_lds_dwordx4 v170, s[82:83]
	s_add_i32 m0, s41, 0xc000
	s_nop 0
	global_load_lds_dwordx4 v172, s[82:83]
	s_add_i32 m0, s41, 0xe000
	s_nop 0
	global_load_lds_dwordx4 v174, s[82:83]
	s_waitcnt vmcnt(8)
	s_waitcnt lgkmcnt(0)
	s_barrier
	s_setprio 1
	s_waitcnt lgkmcnt(0)
	v_mfma_f32_16x16x128_f8f6f4 v[158:161], v[18:25], v[220:227], 0
	s_add_u32 s48, s2, s44
	s_addc_u32 s49, s3, s45
	s_add_u32 s81, s48, 0x3e800100
	s_addc_u32 s82, s49, 0
	v_mfma_f32_16x16x128_f8f6f4 v[154:157], v[26:33], v[220:227], 0
	s_and_b64 s[48:49], s[46:47], exec
	s_cselect_b32 s49, s9, s82
	s_cselect_b32 s48, s8, s81
	s_add_u32 s81, s35, s44
	v_mfma_f32_16x16x128_f8f6f4 v[150:153], v[18:25], v[228:235], 0
	s_addc_u32 s82, s37, s45
	s_and_b64 s[46:47], s[46:47], exec
	s_cselect_b32 s47, s39, s82
	s_cselect_b32 s46, s38, s81
	v_mfma_f32_16x16x128_f8f6f4 v[146:149], v[26:33], v[228:235], 0
	v_mfma_f32_16x16x128_f8f6f4 v[142:145], v[18:25], v[236:243], 0
	v_mfma_f32_16x16x128_f8f6f4 v[138:141], v[26:33], v[236:243], 0
	v_mfma_f32_16x16x128_f8f6f4 v[134:137], v[18:25], v[244:251], 0
	v_mfma_f32_16x16x128_f8f6f4 v[130:133], v[26:33], v[244:251], 0
	s_setprio 0
	s_setprio 1
	v_mfma_f32_16x16x128_f8f6f4 v[102:105], v[2:9], v[220:227], 0
	v_mfma_f32_16x16x128_f8f6f4 v[94:97], v[10:17], v[220:227], 0
	v_mfma_f32_16x16x128_f8f6f4 v[86:89], v[2:9], v[228:235], 0
	v_mfma_f32_16x16x128_f8f6f4 v[82:85], v[10:17], v[228:235], 0
	v_mfma_f32_16x16x128_f8f6f4 v[78:81], v[2:9], v[236:243], 0
	v_mfma_f32_16x16x128_f8f6f4 v[74:77], v[10:17], v[236:243], 0
	v_mfma_f32_16x16x128_f8f6f4 v[70:73], v[2:9], v[244:251], 0
	v_mfma_f32_16x16x128_f8f6f4 v[66:69], v[10:17], v[244:251], 0
	s_setprio 0
	s_barrier
	s_add_i32 s81, s66, s51
	s_mov_b32 m0, s81
	ds_read_b128 v[220:223], v213 offset:16384
	ds_read_b128 v[228:231], v213 offset:18432
	ds_read_b128 v[224:227], v214 offset:16384
	ds_read_b128 v[232:235], v214 offset:18432
	ds_read_b128 v[236:239], v213 offset:20480
	ds_read_b128 v[244:247], v213 offset:22528
	ds_read_b128 v[240:243], v214 offset:20480
	ds_read_b128 v[248:251], v214 offset:22528
	global_load_lds_dwordx4 v162, s[46:47]
	s_add_i32 m0, s81, 0x2000
	s_add_u32 s82, s46, 0x40000
	s_addc_u32 s83, s47, 0
	s_add_i32 s81, s68, s51
	global_load_lds_dwordx4 v164, s[46:47]
	s_mov_b32 m0, s81
	s_nop 0
	global_load_lds_dwordx4 v162, s[82:83]
	s_add_i32 m0, s81, 0x2000
	s_nop 0
	global_load_lds_dwordx4 v164, s[82:83]
	s_waitcnt vmcnt(6)
	s_waitcnt lgkmcnt(0)
	s_barrier
	s_setprio 1
	s_waitcnt lgkmcnt(0)
	v_mfma_f32_16x16x128_f8f6f4 v[126:129], v[18:25], v[220:227], 0
	v_mfma_f32_16x16x128_f8f6f4 v[122:125], v[26:33], v[220:227], 0
	v_mfma_f32_16x16x128_f8f6f4 v[118:121], v[18:25], v[228:235], 0
	v_mfma_f32_16x16x128_f8f6f4 v[114:117], v[26:33], v[228:235], 0
	v_mfma_f32_16x16x128_f8f6f4 v[110:113], v[18:25], v[236:243], 0
	v_mfma_f32_16x16x128_f8f6f4 v[106:109], v[26:33], v[236:243], 0
	v_mfma_f32_16x16x128_f8f6f4 v[98:101], v[18:25], v[244:251], 0
	v_mfma_f32_16x16x128_f8f6f4 v[90:93], v[26:33], v[244:251], 0
	s_setprio 0
	s_setprio 1
	v_mfma_f32_16x16x128_f8f6f4 v[62:65], v[2:9], v[220:227], 0
	v_mfma_f32_16x16x128_f8f6f4 v[58:61], v[10:17], v[220:227], 0
	v_mfma_f32_16x16x128_f8f6f4 v[54:57], v[2:9], v[228:235], 0
	v_mfma_f32_16x16x128_f8f6f4 v[50:53], v[10:17], v[228:235], 0
	v_mfma_f32_16x16x128_f8f6f4 v[46:49], v[2:9], v[236:243], 0
	v_mfma_f32_16x16x128_f8f6f4 v[42:45], v[10:17], v[236:243], 0
	v_mfma_f32_16x16x128_f8f6f4 v[38:41], v[2:9], v[244:251], 0
	v_mfma_f32_16x16x128_f8f6f4 v[34:37], v[10:17], v[244:251], 0
	s_setprio 0
	s_barrier
	s_branch .Lp7_blk3

.LBB0_862:
	s_cmp_eq_u32 s44, 0
	s_cbranch_scc1 .Lp7_first
	ds_read_b128 v[18:21], v210
	ds_read_b128 v[22:25], v211
	ds_read_b128 v[26:29], v210 offset:2048
	ds_read_b128 v[30:33], v211 offset:2048
	ds_read_b128 v[2:5], v210 offset:16384
	ds_read_b128 v[6:9], v211 offset:16384
	ds_read_b128 v[10:13], v210 offset:18432
	ds_read_b128 v[14:17], v211 offset:18432
	s_add_u32 s82, s20, s44
	s_addc_u32 s83, s21, s45
	s_add_i32 m0, s41, 0x8000
	ds_read_b128 v[220:223], v213
	ds_read_b128 v[228:231], v213 offset:2048
	ds_read_b128 v[224:227], v214
	ds_read_b128 v[232:235], v214 offset:2048
	ds_read_b128 v[236:239], v213 offset:4096
	ds_read_b128 v[244:247], v213 offset:6144
	ds_read_b128 v[240:243], v214 offset:4096
	ds_read_b128 v[248:251], v214 offset:6144
	global_load_lds_dwordx4 v166, s[82:83]
	s_add_i32 m0, s41, 0xa000
	s_nop 0
	global_load_lds_dwordx4 v170, s[82:83]
	s_add_i32 m0, s41, 0xc000
	s_nop 0
	global_load_lds_dwordx4 v172, s[82:83]
	s_add_i32 m0, s41, 0xe000
	s_nop 0
	global_load_lds_dwordx4 v174, s[82:83]
	s_waitcnt vmcnt(8)
	s_waitcnt lgkmcnt(0)
	s_barrier
	s_setprio 1
	s_waitcnt lgkmcnt(0)
	v_mfma_f32_16x16x128_f8f6f4 v[158:161], v[18:25], v[220:227], v[158:161]
	s_add_u32 s48, s2, s44
	s_addc_u32 s49, s3, s45
	s_add_u32 s81, s48, 0x3e800100
	s_addc_u32 s82, s49, 0
	v_mfma_f32_16x16x128_f8f6f4 v[154:157], v[26:33], v[220:227], v[154:157]
	s_and_b64 s[48:49], s[46:47], exec
	s_cselect_b32 s49, s9, s82
	s_cselect_b32 s48, s8, s81
	s_add_u32 s81, s35, s44
	v_mfma_f32_16x16x128_f8f6f4 v[150:153], v[18:25], v[228:235], v[150:153]
	s_addc_u32 s82, s37, s45
	s_and_b64 s[46:47], s[46:47], exec
	s_cselect_b32 s47, s39, s82
	s_cselect_b32 s46, s38, s81
	v_mfma_f32_16x16x128_f8f6f4 v[146:149], v[26:33], v[228:235], v[146:149]
	v_mfma_f32_16x16x128_f8f6f4 v[142:145], v[18:25], v[236:243], v[142:145]
	v_mfma_f32_16x16x128_f8f6f4 v[138:141], v[26:33], v[236:243], v[138:141]
	v_mfma_f32_16x16x128_f8f6f4 v[134:137], v[18:25], v[244:251], v[134:137]
	v_mfma_f32_16x16x128_f8f6f4 v[130:133], v[26:33], v[244:251], v[130:133]
	s_setprio 0
	s_setprio 1
	v_mfma_f32_16x16x128_f8f6f4 v[102:105], v[2:9], v[220:227], v[102:105]
	v_mfma_f32_16x16x128_f8f6f4 v[94:97], v[10:17], v[220:227], v[94:97]
	v_mfma_f32_16x16x128_f8f6f4 v[86:89], v[2:9], v[228:235], v[86:89]
	v_mfma_f32_16x16x128_f8f6f4 v[82:85], v[10:17], v[228:235], v[82:85]
	v_mfma_f32_16x16x128_f8f6f4 v[78:81], v[2:9], v[236:243], v[78:81]
	v_mfma_f32_16x16x128_f8f6f4 v[74:77], v[10:17], v[236:243], v[74:77]
	v_mfma_f32_16x16x128_f8f6f4 v[70:73], v[2:9], v[244:251], v[70:73]
	v_mfma_f32_16x16x128_f8f6f4 v[66:69], v[10:17], v[244:251], v[66:69]
	s_setprio 0
	s_barrier
	s_add_i32 s81, s66, s51
	s_mov_b32 m0, s81
	ds_read_b128 v[220:223], v213 offset:16384
	ds_read_b128 v[228:231], v213 offset:18432
	ds_read_b128 v[224:227], v214 offset:16384
	ds_read_b128 v[232:235], v214 offset:18432
	ds_read_b128 v[236:239], v213 offset:20480
	ds_read_b128 v[244:247], v213 offset:22528
	ds_read_b128 v[240:243], v214 offset:20480
	ds_read_b128 v[248:251], v214 offset:22528
	global_load_lds_dwordx4 v162, s[46:47]
	s_add_i32 m0, s81, 0x2000
	s_add_u32 s82, s46, 0x40000
	s_addc_u32 s83, s47, 0
	s_add_i32 s81, s68, s51
	global_load_lds_dwordx4 v164, s[46:47]
	s_mov_b32 m0, s81
	s_nop 0
	global_load_lds_dwordx4 v162, s[82:83]
	s_add_i32 m0, s81, 0x2000
	s_nop 0
	global_load_lds_dwordx4 v164, s[82:83]
	s_waitcnt vmcnt(6)
	s_waitcnt lgkmcnt(0)
	s_barrier
	s_setprio 1
	s_waitcnt lgkmcnt(0)
	v_mfma_f32_16x16x128_f8f6f4 v[126:129], v[18:25], v[220:227], v[126:129]
	v_mfma_f32_16x16x128_f8f6f4 v[122:125], v[26:33], v[220:227], v[122:125]
	v_mfma_f32_16x16x128_f8f6f4 v[118:121], v[18:25], v[228:235], v[118:121]
	v_mfma_f32_16x16x128_f8f6f4 v[114:117], v[26:33], v[228:235], v[114:117]
	v_mfma_f32_16x16x128_f8f6f4 v[110:113], v[18:25], v[236:243], v[110:113]
	v_mfma_f32_16x16x128_f8f6f4 v[106:109], v[26:33], v[236:243], v[106:109]
	v_mfma_f32_16x16x128_f8f6f4 v[98:101], v[18:25], v[244:251], v[98:101]
	v_mfma_f32_16x16x128_f8f6f4 v[90:93], v[26:33], v[244:251], v[90:93]
	s_setprio 0
	s_setprio 1
	v_mfma_f32_16x16x128_f8f6f4 v[62:65], v[2:9], v[220:227], v[62:65]
	v_mfma_f32_16x16x128_f8f6f4 v[58:61], v[10:17], v[220:227], v[58:61]
	v_mfma_f32_16x16x128_f8f6f4 v[54:57], v[2:9], v[228:235], v[54:57]
	v_mfma_f32_16x16x128_f8f6f4 v[50:53], v[10:17], v[228:235], v[50:53]
	v_mfma_f32_16x16x128_f8f6f4 v[46:49], v[2:9], v[236:243], v[46:49]
	v_mfma_f32_16x16x128_f8f6f4 v[42:45], v[10:17], v[236:243], v[42:45]
	v_mfma_f32_16x16x128_f8f6f4 v[38:41], v[2:9], v[244:251], v[38:41]
	v_mfma_f32_16x16x128_f8f6f4 v[34:37], v[10:17], v[244:251], v[34:37]
	s_setprio 0
	s_barrier
.Lp7_blk3:
	ds_read_b128 v[2:5], v210 offset:32768
	ds_read_b128 v[6:9], v211 offset:32768
	ds_read_b128 v[10:13], v210 offset:34816
	ds_read_b128 v[14:17], v211 offset:34816
	ds_read_b128 v[18:21], v210 offset:49152
	ds_read_b128 v[22:25], v211 offset:49152
	ds_read_b128 v[26:29], v210 offset:51200
	ds_read_b128 v[30:33], v211 offset:51200
	s_mov_b32 m0, s41
	ds_read_b128 v[220:223], v213 offset:32768
	ds_read_b128 v[228:231], v213 offset:34816
	ds_read_b128 v[224:227], v214 offset:32768
	ds_read_b128 v[232:235], v214 offset:34816
	ds_read_b128 v[236:239], v213 offset:36864
	ds_read_b128 v[244:247], v213 offset:38912
	ds_read_b128 v[240:243], v214 offset:36864
	ds_read_b128 v[248:251], v214 offset:38912
	global_load_lds_dwordx4 v198, s[48:49]
	s_mov_b32 m0, s53
	s_nop 0
	global_load_lds_dwordx4 v196, s[48:49]
	s_mov_b32 m0, s54
	s_nop 0
	global_load_lds_dwordx4 v194, s[48:49]
	s_mov_b32 m0, s55
	s_nop 0
	global_load_lds_dwordx4 v192, s[48:49]
	s_waitcnt vmcnt(8)
	s_waitcnt lgkmcnt(0)
	s_barrier
	s_setprio 1
	s_waitcnt lgkmcnt(0)
	v_mfma_f32_16x16x128_f8f6f4 v[158:161], v[2:9], v[220:227], v[158:161]
	v_mfma_f32_16x16x128_f8f6f4 v[154:157], v[10:17], v[220:227], v[154:157]
	v_mfma_f32_16x16x128_f8f6f4 v[150:153], v[2:9], v[228:235], v[150:153]
	v_mfma_f32_16x16x128_f8f6f4 v[146:149], v[10:17], v[228:235], v[146:149]
	v_mfma_f32_16x16x128_f8f6f4 v[142:145], v[2:9], v[236:243], v[142:145]
	v_mfma_f32_16x16x128_f8f6f4 v[138:141], v[10:17], v[236:243], v[138:141]
	v_mfma_f32_16x16x128_f8f6f4 v[134:137], v[2:9], v[244:251], v[134:137]
	v_mfma_f32_16x16x128_f8f6f4 v[130:133], v[10:17], v[244:251], v[130:133]
	s_setprio 0
	s_setprio 1
	v_mfma_f32_16x16x128_f8f6f4 v[102:105], v[18:25], v[220:227], v[102:105]
	v_mfma_f32_16x16x128_f8f6f4 v[94:97], v[26:33], v[220:227], v[94:97]
	v_mfma_f32_16x16x128_f8f6f4 v[86:89], v[18:25], v[228:235], v[86:89]
	v_mfma_f32_16x16x128_f8f6f4 v[82:85], v[26:33], v[228:235], v[82:85]
	v_mfma_f32_16x16x128_f8f6f4 v[78:81], v[18:25], v[236:243], v[78:81]
	v_mfma_f32_16x16x128_f8f6f4 v[74:77], v[26:33], v[236:243], v[74:77]
	v_mfma_f32_16x16x128_f8f6f4 v[70:73], v[18:25], v[244:251], v[70:73]
	v_mfma_f32_16x16x128_f8f6f4 v[66:69], v[26:33], v[244:251], v[66:69]
	s_setprio 0
	s_barrier
	s_add_i32 s48, s70, s51
	s_add_u32 s82, s46, s10
	s_addc_u32 s83, s47, s11
	s_mov_b32 m0, s48
	ds_read_b128 v[192:195], v213 offset:49152
	ds_read_b128 v[220:223], v213 offset:51200
	ds_read_b128 v[196:199], v214 offset:49152
	ds_read_b128 v[224:227], v214 offset:51200
	ds_read_b128 v[228:231], v213 offset:53248
	ds_read_b128 v[236:239], v213 offset:55296
	ds_read_b128 v[232:235], v214 offset:53248
	ds_read_b128 v[240:243], v214 offset:55296
	global_load_lds_dwordx4 v162, s[82:83]
	s_add_i32 m0, s48, 0x2000
	s_add_u32 s46, s46, 0x40080
	s_addc_u32 s47, s47, 0
	s_add_i32 s48, s72, s51
	global_load_lds_dwordx4 v164, s[82:83]
	s_mov_b32 m0, s48
	s_nop 0
	global_load_lds_dwordx4 v162, s[46:47]
	s_add_i32 m0, s48, 0x2000
	s_nop 0
	global_load_lds_dwordx4 v164, s[46:47]
	s_waitcnt vmcnt(6)
	s_waitcnt lgkmcnt(0)
	s_barrier
	s_setprio 1
	s_waitcnt lgkmcnt(0)
	v_mfma_f32_16x16x128_f8f6f4 v[126:129], v[2:9], v[192:199], v[126:129]
	v_mfma_f32_16x16x128_f8f6f4 v[122:125], v[10:17], v[192:199], v[122:125]
	v_mfma_f32_16x16x128_f8f6f4 v[118:121], v[2:9], v[220:227], v[118:121]
	v_mfma_f32_16x16x128_f8f6f4 v[114:117], v[10:17], v[220:227], v[114:117]
	v_mfma_f32_16x16x128_f8f6f4 v[110:113], v[2:9], v[228:235], v[110:113]
	v_mfma_f32_16x16x128_f8f6f4 v[106:109], v[10:17], v[228:235], v[106:109]
	v_mfma_f32_16x16x128_f8f6f4 v[98:101], v[2:9], v[236:243], v[98:101]
	v_mfma_f32_16x16x128_f8f6f4 v[90:93], v[10:17], v[236:243], v[90:93]
	s_setprio 0
	s_setprio 1
	v_mfma_f32_16x16x128_f8f6f4 v[62:65], v[18:25], v[192:199], v[62:65]
	v_mfma_f32_16x16x128_f8f6f4 v[58:61], v[26:33], v[192:199], v[58:61]
	v_mfma_f32_16x16x128_f8f6f4 v[54:57], v[18:25], v[220:227], v[54:57]
	v_mfma_f32_16x16x128_f8f6f4 v[50:53], v[26:33], v[220:227], v[50:53]
	v_mfma_f32_16x16x128_f8f6f4 v[46:49], v[18:25], v[228:235], v[46:49]
	v_mfma_f32_16x16x128_f8f6f4 v[42:45], v[26:33], v[228:235], v[42:45]
	v_mfma_f32_16x16x128_f8f6f4 v[38:41], v[18:25], v[236:243], v[38:41]
	v_mfma_f32_16x16x128_f8f6f4 v[34:37], v[26:33], v[236:243], v[34:37]
	s_setprio 0
	s_barrier
	s_add_i32 s43, s43, 2
	s_add_u32 s44, s44, 0x100
	s_addc_u32 s45, s45, 0
	s_cmp_gt_u32 s43, 13
	s_cbranch_scc1 .LBB0_866
